# k6 router staging loads batched, k10 per-expert count loads issued together
# speedup vs baseline: 1.0230x; 1.0018x over previous
; __global__ void __launch_bounds__(NWAVES * 64, 2) fwd(Params P) {
;     ...
;             if (moe) { const float* router = INP(31) + (size_t)li * D * NE;
;                 for (int i = tid; i < D * NE; i += 512) rs[(i & 7) * D + (i >> 3)] = router[i];
;                 if (tid < 16) wgcnt[tid] = 0;
;                 __syncthreads(); }
.LBB0_1192:
	v_ashrrev_i32_e32 v73, 31, v71
	v_mov_b32_e32 v72, v71
	v_ashrrev_i32_e32 v77, 31, v70
	v_mov_b32_e32 v76, v70
	v_lshl_add_u64 v[76:77], v[76:77], 2, s[10:11]
	v_lshl_add_u64 v[72:73], v[72:73], 2, s[10:11]
	global_load_dword v184, v[76:77], off
	s_nop 0
	global_load_dword v185, v[72:73], off
	v_lshlrev_b32_e32 v76, 11, v70
	v_lshlrev_b32_e32 v73, 11, v71
	v_and_b32_e32 v76, 0x3800, v76
	v_and_b32_e32 v73, 0x3800, v73
	v_ashrrev_i32_e32 v78, 3, v70
	v_lshl_add_u32 v82, v76, 2, 0
	v_ashrrev_i32_e32 v77, 3, v71
	v_lshl_add_u32 v83, v73, 2, 0
	v_lshl_add_u32 v192, v78, 2, v82
	v_lshl_add_u32 v193, v77, 2, v83
	v_add_u32_e32 v69, -4, v69
	v_cmp_eq_u32_e32 vcc, 0, v69
	s_or_b64 s[14:15], vcc, s[14:15]
	v_add_u32_e32 v72, 0x400, v70
	v_add_u32_e32 v76, 0x400, v71
	v_ashrrev_i32_e32 v73, 31, v72
	v_ashrrev_i32_e32 v77, 31, v76
	v_lshl_add_u64 v[78:79], v[72:73], 2, s[10:11]
	v_lshl_add_u64 v[80:81], v[76:77], 2, s[10:11]
	global_load_dword v186, v[78:79], off
	global_load_dword v187, v[80:81], off
	v_ashrrev_i32_e32 v72, 3, v72
	v_ashrrev_i32_e32 v76, 3, v76
	v_lshl_add_u32 v194, v72, 2, v82
	v_lshl_add_u32 v195, v76, 2, v83
	v_add_u32_e32 v72, 0x800, v70
	v_add_u32_e32 v76, 0x800, v71
	v_ashrrev_i32_e32 v73, 31, v72
	v_ashrrev_i32_e32 v77, 31, v76
	v_lshl_add_u64 v[78:79], v[72:73], 2, s[10:11]
	v_lshl_add_u64 v[80:81], v[76:77], 2, s[10:11]
	global_load_dword v188, v[78:79], off
	global_load_dword v189, v[80:81], off
	v_ashrrev_i32_e32 v72, 3, v72
	v_ashrrev_i32_e32 v76, 3, v76
	v_lshl_add_u32 v196, v72, 2, v82
	v_lshl_add_u32 v197, v76, 2, v83
	v_add_u32_e32 v72, 0xc00, v70
	v_add_u32_e32 v76, 0xc00, v71
	v_ashrrev_i32_e32 v73, 31, v72
	v_ashrrev_i32_e32 v77, 31, v76
	v_lshl_add_u64 v[78:79], v[72:73], 2, s[10:11]
	v_lshl_add_u64 v[80:81], v[76:77], 2, s[10:11]
	global_load_dword v190, v[78:79], off
	global_load_dword v191, v[80:81], off
	v_ashrrev_i32_e32 v72, 3, v72
	v_ashrrev_i32_e32 v76, 3, v76
	v_lshl_add_u32 v198, v72, 2, v82
	v_lshl_add_u32 v199, v76, 2, v83
	v_add_u32_e32 v71, 0x1000, v71
	v_add_u32_e32 v70, 0x1000, v70
	s_waitcnt vmcnt(0)
	ds_write_b32 v192, v184
	ds_write_b32 v193, v185
	ds_write_b32 v194, v186
	ds_write_b32 v195, v187
	ds_write_b32 v196, v188
	ds_write_b32 v197, v189
	ds_write_b32 v198, v190
	ds_write_b32 v199, v191
	s_andn2_b64 exec, exec, s[14:15]
	s_cbranch_execnz .LBB0_1192
	s_or_b64 exec, exec, s[14:15]

; __global__ void __launch_bounds__(NWAVES * 64, 2) fwd(Params P) {
;     ...
;             int pstart[8]; { int acc_ = 0;
; #pragma unroll
;                 for (int e = 0; e < 8; ++e) { pstart[e] = acc_; acc_ += moe ? (((cnt[e] + 255) >> 8) << 8) : 0; } }
.LBB0_1785:
	v_readlane_b32 s14, v254, 7
	s_and_b64 vcc, exec, s[4:5]
	v_mov_b32_e32 v2, 0
	v_mov_b32_e32 v70, 0
	s_movk_i32 s33, 0x400
	v_readlane_b32 s15, v254, 8
	s_cbranch_vccnz .LBB0_1791
	global_load_dword v70, v3, s[10:11] offset:68
	s_and_b64 vcc, exec, s[4:5]
	s_cbranch_vccz .LBB0_1792

; __global__ void __launch_bounds__(NWAVES * 64, 2) fwd(Params P) {
;     ...
;             int pstart[8]; { int acc_ = 0;
; #pragma unroll
;                 for (int e = 0; e < 8; ++e) { pstart[e] = acc_; acc_ += moe ? (((cnt[e] + 255) >> 8) << 8) : 0; } }
.LBB0_1788:
	global_load_dword v72, v3, s[10:11] offset:76
	s_and_b64 vcc, exec, s[4:5]
	s_cbranch_vccz .LBB0_1794

; __global__ void __launch_bounds__(NWAVES * 64, 2) fwd(Params P) {
;     ...
;             int pstart[8]; { int acc_ = 0;
; #pragma unroll
;                 for (int e = 0; e < 8; ++e) { pstart[e] = acc_; acc_ += moe ? (((cnt[e] + 255) >> 8) << 8) : 0; } }
.LBB0_1790:
	global_load_dword v74, v3, s[10:11] offset:84
	s_and_b64 vcc, exec, s[4:5]
	s_cbranch_vccz .LBB0_1796
	s_branch .LBB0_1797

; __global__ void __launch_bounds__(NWAVES * 64, 2) fwd(Params P) {
;     ...
;             int pstart[8]; { int acc_ = 0;
; #pragma unroll
;                 for (int e = 0; e < 8; ++e) { pstart[e] = acc_; acc_ += moe ? (((cnt[e] + 255) >> 8) << 8) : 0; } }
.LBB0_1792:
	global_load_dword v2, v3, s[10:11] offset:72
	s_and_b64 vcc, exec, s[4:5]
	v_mov_b32_e32 v71, 0
	v_mov_b32_e32 v72, 0
	s_cbranch_vccz .LBB0_1788

; __global__ void __launch_bounds__(NWAVES * 64, 2) fwd(Params P) {
;     ...
;             int pstart[8]; { int acc_ = 0;
; #pragma unroll
;                 for (int e = 0; e < 8; ++e) { pstart[e] = acc_; acc_ += moe ? (((cnt[e] + 255) >> 8) << 8) : 0; } }
.LBB0_1794:
	global_load_dword v71, v3, s[10:11] offset:80
	s_and_b64 vcc, exec, s[4:5]
	v_mov_b32_e32 v73, 0
	v_mov_b32_e32 v74, 0
	s_cbranch_vccz .LBB0_1790

; __global__ void __launch_bounds__(NWAVES * 64, 2) fwd(Params P) {
;     ...
;             int pstart[8]; { int acc_ = 0;
; #pragma unroll
;                 for (int e = 0; e < 8; ++e) { pstart[e] = acc_; acc_ += moe ? (((cnt[e] + 255) >> 8) << 8) : 0; } }
;             for (int m0 = gw; m0 < M; m0 += 2 * NGW) {
;                 const int m1 = m0 + NGW; const bool has1 = m1 < M; const int m1c = has1 ? m1 : m0;
.LBB0_1797:
	s_waitcnt vmcnt(0)
	v_add_u32_e32 v1, 0xff, v1
	v_and_b32_e32 v1, 0xffffff00, v1
	v_add_u32_e32 v70, 0xff, v70
	v_and_b32_e32 v70, 0xffffff00, v70
	v_add_u32_e32 v72, 0xff, v72
	v_and_b32_e32 v72, 0xffffff00, v72
	v_add_u32_e32 v74, 0xff, v74
	v_and_b32_e32 v74, 0xffffff00, v74
	v_add_u32_e32 v2, 0xff, v2
	v_and_b32_e32 v2, 0xffffff00, v2
	v_add_u32_e32 v71, 0xff, v71
	v_and_b32_e32 v71, 0xffffff00, v71
	v_add_u32_e32 v73, 0xff, v73
	v_and_b32_e32 v73, 0xffffff00, v73
	v_readlane_b32 s4, v253, 3
	s_add_i32 s4, s8, s4
	s_ashr_i32 s42, s12, 6
	s_lshl_b32 s43, s4, 3
	s_add_i32 s10, s42, s43
	s_cmpk_lt_i32 s10, 0x4000
	s_cbranch_scc0 .LBB0_1870
	v_readlane_b32 s5, v253, 2
	s_add_i32 s22, s8, s5
	s_and_b64 s[12:13], exec, s[24:25]
	v_readlane_b32 s12, v253, 60
	v_readlane_b32 s13, v253, 61
	s_cselect_b32 s13, s13, 0
	s_cselect_b32 s12, s12, 0
	s_add_u32 s44, s20, 0x16200000
	s_addc_u32 s45, s21, 0
	s_add_u32 s46, s20, 0x16220000
	s_addc_u32 s47, s21, 0
	s_add_u32 s48, s20, 0x16240000
	s_addc_u32 s49, s21, 0
	s_add_u32 s14, s20, 0xa200000
	v_add_u32_e32 v77, v70, v1
	s_addc_u32 s15, s21, 0
	v_add_u32_e32 v79, v2, v77
	s_cmp_eq_u64 s[12:13], 0
	v_add_u32_e32 v81, v72, v79
	s_cselect_b64 s[16:17], -1, 0
	v_lshlrev_b32_e32 v84, 1, v69
	v_mov_b32_e32 v85, v3
	s_lshl_b32 s4, s4, 4
	s_lshl_b32 s5, s42, 1
	v_add_u32_e32 v83, v71, v81
	v_lshl_add_u64 v[70:71], s[20:21], 0, v[84:85]
	s_mov_b64 s[20:21], 0x2a700000
	s_add_i32 s4, s4, s5
	s_lshl_b32 s18, s22, 4
	v_lshl_add_u64 v[88:89], v[70:71], 0, s[20:21]
	s_or_b32 s20, s4, 1
	s_lshl_b32 s4, s8, 4
	v_readlane_b32 s5, v253, 39
	s_ashr_i32 s11, s10, 31
	s_ashr_i32 s19, s18, 31
	s_lshl_b32 s50, s22, 5
	s_add_i32 s51, s5, s4
	v_readlane_b32 s21, v253, 48
	s_add_u32 s21, s21, s8
	v_readlane_b32 s23, v253, 49
	s_mul_i32 s4, s10, 0x1080
	s_addc_u32 s23, s23, s9
	s_mul_hi_i32 s5, s10, 0x1080
	v_and_b32_e32 v68, 63, v68
	s_add_u32 s4, s21, s4
	v_or_b32_e32 v2, 0x400, v69
	v_or_b32_e32 v78, 0x500, v69
	v_or_b32_e32 v80, 0x600, v69
	v_or_b32_e32 v82, 0x700, v69
	v_lshlrev_b32_e32 v68, 3, v68
	v_mov_b32_e32 v69, v3
	s_addc_u32 s5, s23, s5
	v_lshl_add_u64 v[90:91], s[4:5], 0, v[68:69]
	s_lshl_b64 s[24:25], s[10:11], 12
	s_lshl_b64 s[28:29], s[18:19], 12
	v_readlane_b32 s4, v253, 37
	s_add_u32 s4, s4, s8
	v_readlane_b32 s5, v253, 38
	s_addc_u32 s5, s5, s9
	s_add_u32 s4, s4, s24
	v_add_u32_e32 v154, v74, v83
	s_addc_u32 s5, s5, s25
	v_add_u32_e32 v155, v73, v154
	v_lshl_add_u64 v[86:87], s[14:15], 0, v[84:85]
	s_mul_i32 s22, s22, 0x10800
	s_mul_hi_i32 s23, s18, 0x1080
	v_lshl_add_u64 v[92:93], s[4:5], 0, v[68:69]
	s_branch .LBB0_1800
